# down-GEMM: b_down folded into the accumulator init (srcC of first-touch MFMAs), epilogue adds removed
# baseline (speedup 1.0000x reference)
.LBB0_1161:
	s_lshl_b32 s30, s26, 8
	v_readfirstlane_b32 s27, v182
	v_lshrrev_b32_e32 v0, 1, v182
	v_ashrrev_i32_e32 v3, 31, v172
	v_mov_b32_e32 v2, v172
	s_lshr_b32 s31, s27, 1
	s_and_b32 s31, s31, 0x60
	s_or_b32 s30, s31, s30
	v_lshlrev_b64 v[2:3], 12, v[2:3]
	v_and_or_b32 v0, v0, 24, s30
	v_lshl_add_u64 v[2:3], s[40:41], 0, v[2:3]
	v_mov_b32_e32 v1, 0
	v_lshl_add_u64 v[2:3], v[0:1], 2, v[2:3]
	global_load_dwordx4 v[232:235], v[2:3], off
	global_load_dwordx4 v[236:239], v[2:3], off offset:16
	global_load_dwordx4 v[240:243], v[2:3], off offset:512
	global_load_dwordx4 v[244:247], v[2:3], off offset:528
	s_add_i32 s55, s55, 1
	s_lshl_b32 s37, s55, 6
	s_add_i32 s27, s37, s6
	s_cmp_lt_i32 s27, s2
	s_cselect_b64 s[50:51], -1, 0
	s_cmp_ge_i32 s27, s2
	s_cbranch_scc1 .LBB0_1163
	s_lshl_b32 s30, s37, 2
	s_add_i32 s30, s15, s30
	v_mov_b32_e32 v0, s30
	ds_read_b32 v0, v0
	s_mov_b32 s48, s27
	s_waitcnt lgkmcnt(0)
	v_readfirstlane_b32 s46, v0

.Lpeel_down:
	s_add_u32 s30, s72, 0xfffe0080
	s_addc_u32 s31, s73, -1
	s_add_i32 s51, 0, 0x10000
	s_cmp_eq_u32 s50, 4
	s_cselect_b32 s77, s27, s31
	s_cselect_b32 s76, s37, s30
	s_cselect_b32 s75, s65, s49
	s_cselect_b32 s74, s64, s47
	s_add_i32 s58, 0, 0x14000
	v_add_u32_e32 v0, s51, v183
	v_add_u32_e32 v12, s58, v183
	ds_read_b128 v[16:19], v0
	ds_read_b128 v[20:23], v0 offset:1024
	ds_read_b128 v[24:27], v0 offset:2048
	ds_read_b128 v[28:31], v0 offset:3072
	ds_read_b128 v[0:3], v12
	ds_read_b128 v[4:7], v12 offset:1024
	ds_read_b128 v[8:11], v12 offset:2048
	ds_read_b128 v[12:15], v12 offset:3072
	v_lshl_add_u64 v[194:195], s[72:73], 0, v[168:169]
	s_add_i32 m0, s7, 0xc000
	ds_read_b128 v[174:177], v184
	ds_read_b128 v[178:181], v184 offset:1024
	ds_read_b128 v[186:189], v184 offset:2048
	ds_read_b128 v[190:193], v184 offset:3072
	ds_read_b128 v[206:209], v184 offset:4096
	ds_read_b128 v[210:213], v184 offset:5120
	ds_read_b128 v[216:219], v184 offset:6144
	ds_read_b128 v[220:223], v184 offset:7168
	global_load_lds_dwordx4 v[194:195], off
	v_lshl_add_u64 v[194:195], s[72:73], 0, v[170:171]
	s_add_i32 m0, s7, 0xe000
	s_nop 0
	global_load_lds_dwordx4 v[194:195], off
	s_waitcnt vmcnt(2)
	s_waitcnt lgkmcnt(0)
	s_barrier
	s_setprio 1
	s_waitcnt lgkmcnt(0)
	v_mfma_scale_f32_16x16x128_f8f6f4 v[158:161], v[16:23], v[174:181], v[232:235], v200, v201 op_sel_hi:[0,0,0]
	v_mfma_scale_f32_16x16x128_f8f6f4 v[154:157], v[24:31], v[174:181], v[236:239], v200, v201 op_sel_hi:[0,0,0]
	v_mfma_scale_f32_16x16x128_f8f6f4 v[142:145], v[16:23], v[186:193], v[232:235], v200, v201 op_sel_hi:[0,0,0]
	v_mfma_scale_f32_16x16x128_f8f6f4 v[138:141], v[24:31], v[186:193], v[236:239], v200, v201 op_sel_hi:[0,0,0]
	v_mfma_scale_f32_16x16x128_f8f6f4 v[126:129], v[16:23], v[206:213], v[232:235], v200, v201 op_sel_hi:[0,0,0]
	v_mfma_scale_f32_16x16x128_f8f6f4 v[122:125], v[24:31], v[206:213], v[236:239], v200, v201 op_sel_hi:[0,0,0]
	v_mfma_scale_f32_16x16x128_f8f6f4 v[108:111], v[16:23], v[216:223], v[232:235], v200, v201 op_sel_hi:[0,0,0]
	v_mfma_scale_f32_16x16x128_f8f6f4 v[104:107], v[24:31], v[216:223], v[236:239], v200, v201 op_sel_hi:[0,0,0]
	s_setprio 0
	s_setprio 1
	v_mfma_scale_f32_16x16x128_f8f6f4 v[150:153], v[0:7], v[174:181], v[240:243], v200, v201 op_sel_hi:[0,0,0]
	v_mfma_scale_f32_16x16x128_f8f6f4 v[146:149], v[8:15], v[174:181], v[244:247], v200, v201 op_sel_hi:[0,0,0]
	v_mfma_scale_f32_16x16x128_f8f6f4 v[134:137], v[0:7], v[186:193], v[240:243], v200, v201 op_sel_hi:[0,0,0]
	v_mfma_scale_f32_16x16x128_f8f6f4 v[130:133], v[8:15], v[186:193], v[244:247], v200, v201 op_sel_hi:[0,0,0]
	v_mfma_scale_f32_16x16x128_f8f6f4 v[118:121], v[0:7], v[206:213], v[240:243], v200, v201 op_sel_hi:[0,0,0]
	v_mfma_scale_f32_16x16x128_f8f6f4 v[114:117], v[8:15], v[206:213], v[244:247], v200, v201 op_sel_hi:[0,0,0]
	v_mfma_scale_f32_16x16x128_f8f6f4 v[100:103], v[0:7], v[216:223], v[240:243], v200, v201 op_sel_hi:[0,0,0]
	v_mfma_scale_f32_16x16x128_f8f6f4 v[96:99], v[8:15], v[216:223], v[244:247], v200, v201 op_sel_hi:[0,0,0]
	s_setprio 0
	s_barrier
	s_add_i32 s30, s51, s14
	v_lshl_add_u64 v[174:175], s[74:75], 0, v[112:113]
	s_mov_b32 m0, s30
	ds_read_b128 v[186:189], v184 offset:16384
	ds_read_b128 v[190:193], v184 offset:17408
	ds_read_b128 v[206:209], v184 offset:18432
	ds_read_b128 v[210:213], v184 offset:19456
	ds_read_b128 v[216:219], v184 offset:20480
	ds_read_b128 v[220:223], v184 offset:21504
	ds_read_b128 v[224:227], v184 offset:22528
	ds_read_b128 v[228:231], v184 offset:23552
	global_load_lds_dwordx4 v[174:175], off
	s_add_i32 m0, s30, 0x2000
	s_add_u32 s30, s74, 0x20000
	v_lshl_add_u64 v[176:177], s[74:75], 0, v[162:163]
	s_addc_u32 s31, s75, 0
	s_add_i32 s45, s58, s14
	global_load_lds_dwordx4 v[176:177], off
	v_lshl_add_u64 v[178:179], s[30:31], 0, v[112:113]
	s_mov_b32 m0, s45
	v_lshl_add_u64 v[180:181], s[76:77], 0, v[164:165]
	global_load_lds_dwordx4 v[178:179], off
	v_lshl_add_u64 v[178:179], s[30:31], 0, v[162:163]
	s_add_i32 m0, s45, 0x2000
	s_nop 0
	global_load_lds_dwordx4 v[178:179], off
	v_lshl_add_u64 v[178:179], s[76:77], 0, v[166:167]
	s_mov_b32 m0, s7
	s_nop 0
	global_load_lds_dwordx4 v[178:179], off
	s_mov_b32 m0, s25
	s_nop 0
	global_load_lds_dwordx4 v[180:181], off
	s_waitcnt vmcnt(8)
	s_waitcnt lgkmcnt(0)
	s_barrier
	s_setprio 1
	s_waitcnt lgkmcnt(0)
	v_mfma_scale_f32_16x16x128_f8f6f4 v[92:95], v[16:23], v[186:193], v[232:235], v200, v201 op_sel_hi:[0,0,0]
	v_mfma_scale_f32_16x16x128_f8f6f4 v[88:91], v[24:31], v[186:193], v[236:239], v200, v201 op_sel_hi:[0,0,0]
	v_mfma_scale_f32_16x16x128_f8f6f4 v[76:79], v[16:23], v[206:213], v[232:235], v200, v201 op_sel_hi:[0,0,0]
	v_mfma_scale_f32_16x16x128_f8f6f4 v[72:75], v[24:31], v[206:213], v[236:239], v200, v201 op_sel_hi:[0,0,0]
	v_mfma_scale_f32_16x16x128_f8f6f4 v[60:63], v[16:23], v[216:223], v[232:235], v200, v201 op_sel_hi:[0,0,0]
	v_mfma_scale_f32_16x16x128_f8f6f4 v[56:59], v[24:31], v[216:223], v[236:239], v200, v201 op_sel_hi:[0,0,0]
	v_mfma_scale_f32_16x16x128_f8f6f4 v[44:47], v[16:23], v[224:231], v[232:235], v200, v201 op_sel_hi:[0,0,0]
	v_mfma_scale_f32_16x16x128_f8f6f4 v[40:43], v[24:31], v[224:231], v[236:239], v200, v201 op_sel_hi:[0,0,0]
	s_setprio 0
	s_setprio 1
	v_mfma_scale_f32_16x16x128_f8f6f4 v[84:87], v[0:7], v[186:193], v[240:243], v200, v201 op_sel_hi:[0,0,0]
	v_mfma_scale_f32_16x16x128_f8f6f4 v[80:83], v[8:15], v[186:193], v[244:247], v200, v201 op_sel_hi:[0,0,0]
	v_mfma_scale_f32_16x16x128_f8f6f4 v[68:71], v[0:7], v[206:213], v[240:243], v200, v201 op_sel_hi:[0,0,0]
	v_mfma_scale_f32_16x16x128_f8f6f4 v[64:67], v[8:15], v[206:213], v[244:247], v200, v201 op_sel_hi:[0,0,0]
	v_mfma_scale_f32_16x16x128_f8f6f4 v[52:55], v[0:7], v[216:223], v[240:243], v200, v201 op_sel_hi:[0,0,0]
	v_mfma_scale_f32_16x16x128_f8f6f4 v[48:51], v[8:15], v[216:223], v[244:247], v200, v201 op_sel_hi:[0,0,0]
	v_mfma_scale_f32_16x16x128_f8f6f4 v[36:39], v[0:7], v[224:231], v[240:243], v200, v201 op_sel_hi:[0,0,0]
	v_mfma_scale_f32_16x16x128_f8f6f4 v[32:35], v[8:15], v[224:231], v[244:247], v200, v201 op_sel_hi:[0,0,0]
	s_setprio 0
	s_barrier
	s_add_i32 s45, 0, 0x18000
	s_add_i32 s51, 0, 0x1c000
	v_add_u32_e32 v12, s45, v183
	v_add_u32_e32 v28, s51, v183
	ds_read_b128 v[0:3], v12
	ds_read_b128 v[4:7], v12 offset:1024
	ds_read_b128 v[8:11], v12 offset:2048
	ds_read_b128 v[12:15], v12 offset:3072
	ds_read_b128 v[16:19], v28
	ds_read_b128 v[20:23], v28 offset:1024
	ds_read_b128 v[24:27], v28 offset:2048
	ds_read_b128 v[28:31], v28 offset:3072
	s_add_u32 s30, s76, 0x20000
	s_addc_u32 s31, s77, 0
	s_mov_b32 m0, s33
	v_lshl_add_u64 v[194:195], s[30:31], 0, v[166:167]
	ds_read_b128 v[186:189], v184 offset:32768
	ds_read_b128 v[190:193], v184 offset:33792
	ds_read_b128 v[206:209], v184 offset:34816
	ds_read_b128 v[210:213], v184 offset:35840
	ds_read_b128 v[216:219], v184 offset:36864
	ds_read_b128 v[220:223], v184 offset:37888
	ds_read_b128 v[224:227], v184 offset:38912
	ds_read_b128 v[228:231], v184 offset:39936
	global_load_lds_dwordx4 v[194:195], off
	v_lshl_add_u64 v[194:195], s[30:31], 0, v[164:165]
	s_mov_b32 m0, s34
	s_nop 0
	global_load_lds_dwordx4 v[194:195], off
	s_waitcnt vmcnt(8)
	s_waitcnt lgkmcnt(0)
	s_barrier
	s_setprio 1
	s_waitcnt lgkmcnt(0)
	v_mfma_scale_f32_16x16x128_f8f6f4 v[158:161], v[0:7], v[186:193], v[158:161], v200, v201 op_sel_hi:[0,0,0]
	v_mfma_scale_f32_16x16x128_f8f6f4 v[154:157], v[8:15], v[186:193], v[154:157], v200, v201 op_sel_hi:[0,0,0]
	v_mfma_scale_f32_16x16x128_f8f6f4 v[142:145], v[0:7], v[206:213], v[142:145], v200, v201 op_sel_hi:[0,0,0]
	v_mfma_scale_f32_16x16x128_f8f6f4 v[138:141], v[8:15], v[206:213], v[138:141], v200, v201 op_sel_hi:[0,0,0]
	v_mfma_scale_f32_16x16x128_f8f6f4 v[126:129], v[0:7], v[216:223], v[126:129], v200, v201 op_sel_hi:[0,0,0]
	v_mfma_scale_f32_16x16x128_f8f6f4 v[122:125], v[8:15], v[216:223], v[122:125], v200, v201 op_sel_hi:[0,0,0]
	v_mfma_scale_f32_16x16x128_f8f6f4 v[108:111], v[0:7], v[224:231], v[108:111], v200, v201 op_sel_hi:[0,0,0]
	v_mfma_scale_f32_16x16x128_f8f6f4 v[104:107], v[8:15], v[224:231], v[104:107], v200, v201 op_sel_hi:[0,0,0]
	s_setprio 0
	s_setprio 1
	v_mfma_scale_f32_16x16x128_f8f6f4 v[150:153], v[16:23], v[186:193], v[150:153], v200, v201 op_sel_hi:[0,0,0]
	v_mfma_scale_f32_16x16x128_f8f6f4 v[146:149], v[24:31], v[186:193], v[146:149], v200, v201 op_sel_hi:[0,0,0]
	v_mfma_scale_f32_16x16x128_f8f6f4 v[134:137], v[16:23], v[206:213], v[134:137], v200, v201 op_sel_hi:[0,0,0]
	v_mfma_scale_f32_16x16x128_f8f6f4 v[130:133], v[24:31], v[206:213], v[130:133], v200, v201 op_sel_hi:[0,0,0]
	v_mfma_scale_f32_16x16x128_f8f6f4 v[118:121], v[16:23], v[216:223], v[118:121], v200, v201 op_sel_hi:[0,0,0]
	v_mfma_scale_f32_16x16x128_f8f6f4 v[114:117], v[24:31], v[216:223], v[114:117], v200, v201 op_sel_hi:[0,0,0]
	v_mfma_scale_f32_16x16x128_f8f6f4 v[100:103], v[16:23], v[224:231], v[100:103], v200, v201 op_sel_hi:[0,0,0]
	v_mfma_scale_f32_16x16x128_f8f6f4 v[96:99], v[24:31], v[224:231], v[96:99], v200, v201 op_sel_hi:[0,0,0]
	s_setprio 0
	s_barrier
	s_add_i32 s30, s45, s14
	v_lshl_add_u64 v[174:175], v[174:175], 0, s[56:57]
	s_mov_b32 m0, s30
	ds_read_b128 v[186:189], v184 offset:49152
	ds_read_b128 v[190:193], v184 offset:50176
	ds_read_b128 v[206:209], v184 offset:51200
	ds_read_b128 v[210:213], v184 offset:52224
	ds_read_b128 v[216:219], v184 offset:53248
	ds_read_b128 v[220:223], v184 offset:54272
	ds_read_b128 v[224:227], v184 offset:55296
	ds_read_b128 v[228:231], v184 offset:56320
	global_load_lds_dwordx4 v[174:175], off
	s_add_i32 m0, s30, 0x2000
	s_add_u32 s30, s74, 0x20080
	v_lshl_add_u64 v[174:175], v[176:177], 0, s[56:57]
	s_addc_u32 s31, s75, 0
	s_add_i32 s45, s51, s14
	global_load_lds_dwordx4 v[174:175], off
	v_lshl_add_u64 v[174:175], s[30:31], 0, v[112:113]
	s_mov_b32 m0, s45
	s_nop 0
	global_load_lds_dwordx4 v[174:175], off
	v_lshl_add_u64 v[174:175], s[30:31], 0, v[162:163]
	s_add_i32 m0, s45, 0x2000
	s_nop 0
	global_load_lds_dwordx4 v[174:175], off
	v_lshl_add_u64 v[174:175], v[178:179], 0, s[56:57]
	s_mov_b32 m0, s4
	s_nop 0
	global_load_lds_dwordx4 v[174:175], off
	v_lshl_add_u64 v[174:175], v[180:181], 0, s[56:57]
	s_mov_b32 m0, s54
	s_nop 0
	global_load_lds_dwordx4 v[174:175], off
	s_waitcnt vmcnt(8)
	s_waitcnt lgkmcnt(0)
	s_barrier
	s_setprio 1
	s_waitcnt lgkmcnt(0)
	v_mfma_scale_f32_16x16x128_f8f6f4 v[92:95], v[0:7], v[186:193], v[92:95], v200, v201 op_sel_hi:[0,0,0]
	v_mfma_scale_f32_16x16x128_f8f6f4 v[88:91], v[8:15], v[186:193], v[88:91], v200, v201 op_sel_hi:[0,0,0]
	v_mfma_scale_f32_16x16x128_f8f6f4 v[76:79], v[0:7], v[206:213], v[76:79], v200, v201 op_sel_hi:[0,0,0]
	v_mfma_scale_f32_16x16x128_f8f6f4 v[72:75], v[8:15], v[206:213], v[72:75], v200, v201 op_sel_hi:[0,0,0]
	v_mfma_scale_f32_16x16x128_f8f6f4 v[60:63], v[0:7], v[216:223], v[60:63], v200, v201 op_sel_hi:[0,0,0]
	v_mfma_scale_f32_16x16x128_f8f6f4 v[56:59], v[8:15], v[216:223], v[56:59], v200, v201 op_sel_hi:[0,0,0]
	v_mfma_scale_f32_16x16x128_f8f6f4 v[44:47], v[0:7], v[224:231], v[44:47], v200, v201 op_sel_hi:[0,0,0]
	v_mfma_scale_f32_16x16x128_f8f6f4 v[40:43], v[8:15], v[224:231], v[40:43], v200, v201 op_sel_hi:[0,0,0]
	s_setprio 0
	s_setprio 1
	v_mfma_scale_f32_16x16x128_f8f6f4 v[84:87], v[16:23], v[186:193], v[84:87], v200, v201 op_sel_hi:[0,0,0]
	v_mfma_scale_f32_16x16x128_f8f6f4 v[80:83], v[24:31], v[186:193], v[80:83], v200, v201 op_sel_hi:[0,0,0]
	v_mfma_scale_f32_16x16x128_f8f6f4 v[68:71], v[16:23], v[206:213], v[68:71], v200, v201 op_sel_hi:[0,0,0]
	v_mfma_scale_f32_16x16x128_f8f6f4 v[64:67], v[24:31], v[206:213], v[64:67], v200, v201 op_sel_hi:[0,0,0]
	v_mfma_scale_f32_16x16x128_f8f6f4 v[52:55], v[16:23], v[216:223], v[52:55], v200, v201 op_sel_hi:[0,0,0]
	v_mfma_scale_f32_16x16x128_f8f6f4 v[48:51], v[24:31], v[216:223], v[48:51], v200, v201 op_sel_hi:[0,0,0]
	v_mfma_scale_f32_16x16x128_f8f6f4 v[36:39], v[16:23], v[224:231], v[36:39], v200, v201 op_sel_hi:[0,0,0]
	v_mfma_scale_f32_16x16x128_f8f6f4 v[32:35], v[24:31], v[224:231], v[32:35], v200, v201 op_sel_hi:[0,0,0]
	s_setprio 0
	s_barrier
	s_add_i32 s50, s50, 2
	s_add_u32 s72, s72, 0x100
	s_addc_u32 s73, s73, 0
	s_add_u32 s47, s47, 0x100
	s_addc_u32 s49, s49, 0
	s_cmp_gt_u32 s50, 5

.LBB0_1169:
	v_mov_b32_e32 v16, v182
	s_nop 15
	s_nop 15
	s_lshl_b32 s30, s26, 8
	v_readfirstlane_b32 s27, v16
	s_lshr_b32 s31, s27, 1
	s_and_b32 s31, s31, 0x60
	s_or_b32 s30, s31, s30
	v_lshrrev_b32_e32 v0, 1, v16
	s_ashr_i32 s27, s27, 2
	v_and_or_b32 v18, v0, 24, s30
	s_lshl_b32 s30, s36, 8
	s_andn2_b32 s27, s27, 63
	v_ashrrev_i32_e32 v173, 31, v172
	s_add_i32 s27, s27, s30
	v_lshlrev_b64 v[0:1], 12, v[172:173]
	v_and_or_b32 v16, v16, 15, s27
	v_readlane_b32 s30, v254, 24
	v_lshl_add_u64 v[0:1], s[40:41], 0, v[0:1]
	v_ashrrev_i32_e32 v19, 31, v18
	v_ashrrev_i32_e32 v17, 31, v16
	v_readlane_b32 s31, v254, 25
	v_lshl_add_u64 v[4:5], v[18:19], 2, v[0:1]
	s_nop 0
	v_lshl_add_u64 v[24:25], v[16:17], 2, s[30:31]
	global_load_dword v30, v[24:25], off
	v_or_b32_e32 v26, 16, v16
	v_ashrrev_i32_e32 v27, 31, v26
	v_lshl_add_u64 v[20:21], v[26:27], 2, s[30:31]
	global_load_dword v178, v[20:21], off
	v_or_b32_e32 v22, 32, v16
	v_ashrrev_i32_e32 v23, 31, v22
	v_lshl_add_u64 v[20:21], v[22:23], 2, s[30:31]
	global_load_dword v177, v[20:21], off
	v_or_b32_e32 v20, 48, v16
	v_ashrrev_i32_e32 v21, 31, v20
	v_lshl_add_u64 v[28:29], v[20:21], 2, s[30:31]
	global_load_dword v176, v[28:29], off
	global_load_dword v175, v[24:25], off offset:512
	global_load_dword v174, v[24:25], off offset:576
	global_load_dword v173, v[24:25], off offset:640
	global_load_dword v172, v[24:25], off offset:704
	v_lshlrev_b64 v[22:23], 10, v[22:23]
	v_lshl_add_u64 v[22:23], s[16:17], 0, v[22:23]
	v_lshl_add_u64 v[22:23], v[22:23], 0, v[18:19]
	v_lshlrev_b64 v[16:17], 10, v[16:17]
	v_lshlrev_b64 v[20:21], 10, v[20:21]
	v_lshl_add_u64 v[16:17], s[16:17], 0, v[16:17]
	v_lshl_add_u64 v[20:21], s[16:17], 0, v[20:21]
	v_lshl_add_u64 v[16:17], v[16:17], 0, v[18:19]
	s_mov_b64 s[30:31], 0x20000
	s_mov_b32 s21, 0x24000
	s_mov_b32 s27, 0x2c000
	s_mov_b64 s[50:51], -1
	v_readlane_b32 s58, v255, 15
	v_readlane_b32 s76, v255, 16
	v_readlane_b32 s77, v255, 18
	s_waitcnt vmcnt(0)
	v_mul_f32_e32 v24, 0x41800000, v30
	v_mov_b64_e32 v[30:31], v[158:159]
	v_mov_b32_e32 v158, v113
	v_pk_mul_f32 v[30:31], v[30:31], v[24:25] op_sel_hi:[1,0]
	v_pk_mul_f32 v[28:29], v[160:161], v[24:25] op_sel_hi:[1,0]
	v_cvt_pk_fp8_f32 v158, v30, v31
	v_pk_mul_f32 v[156:157], v[156:157], v[24:25] op_sel_hi:[1,0]
	v_pk_mul_f32 v[154:155], v[154:155], v[24:25] op_sel_hi:[1,0]
	v_cvt_pk_fp8_f32 v158, v28, v29 op_sel:[0,0,1]
	v_pk_mul_f32 v[30:31], v[150:151], v[24:25] op_sel_hi:[1,0]
	v_pk_mul_f32 v[28:29], v[152:153], v[24:25] op_sel_hi:[1,0]
	v_pk_mul_f32 v[148:149], v[148:149], v[24:25] op_sel_hi:[1,0]
	v_pk_mul_f32 v[24:25], v[146:147], v[24:25] op_sel_hi:[1,0]
	v_mov_b32_e32 v146, v113
	v_cvt_pk_fp8_f32 v146, v30, v31
	v_mov_b64_e32 v[30:31], v[142:143]
	v_mov_b32_e32 v142, v113
	v_mov_b32_e32 v147, v113
	v_cvt_pk_fp8_f32 v146, v28, v29 op_sel:[0,0,1]
	v_mul_f32_e32 v28, 0x41800000, v178
	v_pk_mul_f32 v[30:31], v[30:31], v[28:29] op_sel_hi:[1,0]
	v_cvt_pk_fp8_f32 v147, v24, v25
	v_cvt_pk_fp8_f32 v142, v30, v31
	v_lshlrev_b64 v[24:25], 10, v[26:27]
	v_pk_mul_f32 v[26:27], v[144:145], v[28:29] op_sel_hi:[1,0]
	v_cvt_pk_fp8_f32 v142, v26, v27 op_sel:[0,0,1]
	v_pk_mul_f32 v[30:31], v[136:137], v[28:29] op_sel_hi:[1,0]
	v_pk_mul_f32 v[140:141], v[140:141], v[28:29] op_sel_hi:[1,0]
	v_pk_mul_f32 v[138:139], v[138:139], v[28:29] op_sel_hi:[1,0]
	v_mov_b32_e32 v143, v113
	v_pk_mul_f32 v[134:135], v[134:135], v[28:29] op_sel_hi:[1,0]
	v_pk_mul_f32 v[26:27], v[132:133], v[28:29] op_sel_hi:[1,0]
	v_pk_mul_f32 v[28:29], v[130:131], v[28:29] op_sel_hi:[1,0]
	v_mov_b32_e32 v130, v113
	v_mov_b32_e32 v131, v113
	v_cvt_pk_fp8_f32 v143, v138, v139
	v_cvt_pk_fp8_f32 v130, v134, v135
	v_cvt_pk_fp8_f32 v131, v28, v29
	v_lshl_add_u64 v[24:25], s[16:17], 0, v[24:25]
	v_cvt_pk_fp8_f32 v143, v140, v141 op_sel:[0,0,1]
	v_cvt_pk_fp8_f32 v130, v30, v31 op_sel:[0,0,1]
	v_cvt_pk_fp8_f32 v131, v26, v27 op_sel:[0,0,1]
	v_lshl_add_u64 v[24:25], v[24:25], 0, v[18:19]
	global_store_dwordx2 v[24:25], v[142:143], off
	global_store_dwordx2 v[24:25], v[130:131], off offset:128
	v_mul_f32_e32 v24, 0x41800000, v177
	v_pk_mul_f32 v[28:29], v[126:127], v[24:25] op_sel_hi:[1,0]
	v_mov_b64_e32 v[30:31], v[124:125]
	v_pk_mul_f32 v[122:123], v[122:123], v[24:25] op_sel_hi:[1,0]
	v_mov_b32_e32 v124, v113
	v_mov_b32_e32 v125, v113
	v_cvt_pk_fp8_f32 v124, v28, v29
	v_cvt_pk_fp8_f32 v125, v122, v123
	v_pk_mul_f32 v[30:31], v[30:31], v[24:25] op_sel_hi:[1,0]
	v_pk_mul_f32 v[26:27], v[128:129], v[24:25] op_sel_hi:[1,0]
	v_cvt_pk_fp8_f32 v125, v30, v31 op_sel:[0,0,1]
	v_cvt_pk_fp8_f32 v124, v26, v27 op_sel:[0,0,1]
	v_pk_mul_f32 v[26:27], v[120:121], v[24:25] op_sel_hi:[1,0]
	v_pk_mul_f32 v[28:29], v[118:119], v[24:25] op_sel_hi:[1,0]
	v_pk_mul_f32 v[30:31], v[116:117], v[24:25] op_sel_hi:[1,0]
	v_pk_mul_f32 v[24:25], v[114:115], v[24:25] op_sel_hi:[1,0]
	v_mov_b32_e32 v114, v113
	v_mov_b32_e32 v115, v113
	v_cvt_pk_fp8_f32 v114, v28, v29
	v_cvt_pk_fp8_f32 v115, v24, v25
	global_store_dwordx2 v[22:23], v[124:125], off
	v_cvt_pk_fp8_f32 v114, v26, v27 op_sel:[0,0,1]
	v_cvt_pk_fp8_f32 v115, v30, v31 op_sel:[0,0,1]
	v_mov_b32_e32 v30, v113
	v_mov_b32_e32 v31, v113
	global_store_dwordx2 v[22:23], v[114:115], off offset:128
	v_mul_f32_e32 v22, 0x41800000, v176
	v_pk_mul_f32 v[24:25], v[108:109], v[22:23] op_sel_hi:[1,0]
	v_pk_mul_f32 v[28:29], v[104:105], v[22:23] op_sel_hi:[1,0]
	v_cvt_pk_fp8_f32 v30, v24, v25
	v_cvt_pk_fp8_f32 v31, v28, v29
	v_lshl_add_u64 v[18:19], v[20:21], 0, v[18:19]
	v_pk_mul_f32 v[20:21], v[110:111], v[22:23] op_sel_hi:[1,0]
	v_pk_mul_f32 v[26:27], v[106:107], v[22:23] op_sel_hi:[1,0]
	v_cvt_pk_fp8_f32 v30, v20, v21 op_sel:[0,0,1]
	v_cvt_pk_fp8_f32 v31, v26, v27 op_sel:[0,0,1]
	v_pk_mul_f32 v[20:21], v[102:103], v[22:23] op_sel_hi:[1,0]
	v_pk_mul_f32 v[24:25], v[100:101], v[22:23] op_sel_hi:[1,0]
	v_pk_mul_f32 v[26:27], v[98:99], v[22:23] op_sel_hi:[1,0]
	v_pk_mul_f32 v[22:23], v[96:97], v[22:23] op_sel_hi:[1,0]
	v_mov_b32_e32 v28, v113
	v_mov_b32_e32 v29, v113
	v_cvt_pk_fp8_f32 v28, v24, v25
	v_cvt_pk_fp8_f32 v29, v22, v23
	global_store_dwordx2 v[18:19], v[30:31], off
	v_cvt_pk_fp8_f32 v28, v20, v21 op_sel:[0,0,1]
	v_cvt_pk_fp8_f32 v29, v26, v27 op_sel:[0,0,1]
	v_mov_b32_e32 v30, v113
	v_mov_b32_e32 v31, v113
	global_store_dwordx2 v[18:19], v[28:29], off offset:128
	v_mul_f32_e32 v18, 0x41800000, v175
	v_pk_mul_f32 v[24:25], v[92:93], v[18:19] op_sel_hi:[1,0]
	v_pk_mul_f32 v[28:29], v[88:89], v[18:19] op_sel_hi:[1,0]
	v_cvt_pk_fp8_f32 v30, v24, v25
	v_cvt_pk_fp8_f32 v31, v28, v29
	v_pk_mul_f32 v[22:23], v[94:95], v[18:19] op_sel_hi:[1,0]
	v_pk_mul_f32 v[26:27], v[90:91], v[18:19] op_sel_hi:[1,0]
	v_cvt_pk_fp8_f32 v30, v22, v23 op_sel:[0,0,1]
	v_cvt_pk_fp8_f32 v31, v26, v27 op_sel:[0,0,1]
	v_add_co_u32_e32 v22, vcc, s63, v16
	s_nop 0
	v_addc_co_u32_e32 v23, vcc, 0, v17, vcc
	global_store_dwordx2 v[22:23], v[30:31], off
	v_pk_mul_f32 v[22:23], v[86:87], v[18:19] op_sel_hi:[1,0]
	v_pk_mul_f32 v[24:25], v[84:85], v[18:19] op_sel_hi:[1,0]
	v_pk_mul_f32 v[26:27], v[82:83], v[18:19] op_sel_hi:[1,0]
	v_pk_mul_f32 v[18:19], v[80:81], v[18:19] op_sel_hi:[1,0]
	v_mov_b32_e32 v28, v113
	v_mov_b32_e32 v29, v113
	v_cvt_pk_fp8_f32 v28, v24, v25
	v_cvt_pk_fp8_f32 v29, v18, v19
	v_lshl_add_u64 v[20:21], v[16:17], 0, s[30:31]
	v_mul_f32_e32 v18, 0x41800000, v174
	v_cvt_pk_fp8_f32 v28, v22, v23 op_sel:[0,0,1]
	v_cvt_pk_fp8_f32 v29, v26, v27 op_sel:[0,0,1]
	v_mov_b32_e32 v30, v113
	v_pk_mul_f32 v[24:25], v[76:77], v[18:19] op_sel_hi:[1,0]
	global_store_dwordx2 v[20:21], v[28:29], off offset:128
	v_mov_b32_e32 v31, v113
	v_pk_mul_f32 v[28:29], v[72:73], v[18:19] op_sel_hi:[1,0]
	v_cvt_pk_fp8_f32 v30, v24, v25
	v_cvt_pk_fp8_f32 v31, v28, v29
	v_pk_mul_f32 v[22:23], v[78:79], v[18:19] op_sel_hi:[1,0]
	v_pk_mul_f32 v[26:27], v[74:75], v[18:19] op_sel_hi:[1,0]
	v_cvt_pk_fp8_f32 v30, v22, v23 op_sel:[0,0,1]
	v_cvt_pk_fp8_f32 v31, v26, v27 op_sel:[0,0,1]
	v_add_co_u32_e32 v22, vcc, s21, v16
	s_nop 0
	v_addc_co_u32_e32 v23, vcc, 0, v17, vcc
	global_store_dwordx2 v[22:23], v[30:31], off
	v_pk_mul_f32 v[22:23], v[70:71], v[18:19] op_sel_hi:[1,0]
	v_pk_mul_f32 v[24:25], v[68:69], v[18:19] op_sel_hi:[1,0]
	v_pk_mul_f32 v[26:27], v[66:67], v[18:19] op_sel_hi:[1,0]
	v_pk_mul_f32 v[18:19], v[64:65], v[18:19] op_sel_hi:[1,0]
	v_mov_b32_e32 v28, v113
	v_mov_b32_e32 v29, v113
	v_cvt_pk_fp8_f32 v28, v24, v25
	v_cvt_pk_fp8_f32 v29, v18, v19
	s_mov_b64 s[30:31], 0x24000
	v_lshl_add_u64 v[20:21], v[16:17], 0, s[30:31]
	v_cvt_pk_fp8_f32 v28, v22, v23 op_sel:[0,0,1]
	v_cvt_pk_fp8_f32 v29, v26, v27 op_sel:[0,0,1]
	v_mul_f32_e32 v18, 0x41800000, v173
	v_mov_b32_e32 v30, v113
	global_store_dwordx2 v[20:21], v[28:29], off offset:128
	v_pk_mul_f32 v[24:25], v[60:61], v[18:19] op_sel_hi:[1,0]
	v_pk_mul_f32 v[28:29], v[56:57], v[18:19] op_sel_hi:[1,0]
	v_mov_b32_e32 v31, v113
	v_cvt_pk_fp8_f32 v30, v24, v25
	v_cvt_pk_fp8_f32 v31, v28, v29
	v_pk_mul_f32 v[22:23], v[62:63], v[18:19] op_sel_hi:[1,0]
	v_pk_mul_f32 v[26:27], v[58:59], v[18:19] op_sel_hi:[1,0]
	v_cvt_pk_fp8_f32 v30, v22, v23 op_sel:[0,0,1]
	v_cvt_pk_fp8_f32 v31, v26, v27 op_sel:[0,0,1]
	s_mov_b32 s21, 0x28000
	v_add_co_u32_e32 v22, vcc, s21, v16
	s_nop 0
	v_addc_co_u32_e32 v23, vcc, 0, v17, vcc
	global_store_dwordx2 v[22:23], v[30:31], off
	v_pk_mul_f32 v[22:23], v[54:55], v[18:19] op_sel_hi:[1,0]
	v_pk_mul_f32 v[24:25], v[52:53], v[18:19] op_sel_hi:[1,0]
	v_pk_mul_f32 v[26:27], v[50:51], v[18:19] op_sel_hi:[1,0]
	v_pk_mul_f32 v[18:19], v[48:49], v[18:19] op_sel_hi:[1,0]
	v_mov_b32_e32 v28, v113
	v_cvt_pk_fp8_f32 v28, v24, v25
	v_mov_b32_e32 v29, v113
	v_cvt_pk_fp8_f32 v29, v18, v19
	v_mul_f32_e32 v18, 0x41800000, v172
	v_cvt_pk_fp8_f32 v28, v22, v23 op_sel:[0,0,1]
	v_pk_mul_f32 v[12:13], v[44:45], v[18:19] op_sel_hi:[1,0]
	v_pk_mul_f32 v[8:9], v[40:41], v[18:19] op_sel_hi:[1,0]
	v_mov_b32_e32 v22, v113
	v_mov_b32_e32 v23, v113
	v_cvt_pk_fp8_f32 v22, v12, v13
	v_cvt_pk_fp8_f32 v23, v8, v9
	v_pk_mul_f32 v[14:15], v[46:47], v[18:19] op_sel_hi:[1,0]
	v_pk_mul_f32 v[10:11], v[42:43], v[18:19] op_sel_hi:[1,0]
	v_cvt_pk_fp8_f32 v22, v14, v15 op_sel:[0,0,1]
	v_cvt_pk_fp8_f32 v23, v10, v11 op_sel:[0,0,1]
	v_add_co_u32_e32 v8, vcc, s27, v16
	s_nop 0
	v_addc_co_u32_e32 v9, vcc, 0, v17, vcc
	v_mov_b32_e32 v159, v113
	global_store_dwordx2 v[8:9], v[22:23], off
	v_pk_mul_f32 v[4:5], v[36:37], v[18:19] op_sel_hi:[1,0]
	v_pk_mul_f32 v[0:1], v[32:33], v[18:19] op_sel_hi:[1,0]
	v_mov_b32_e32 v8, v113
	v_mov_b32_e32 v9, v113
	v_cvt_pk_fp8_f32 v159, v154, v155
	v_cvt_pk_fp8_f32 v8, v4, v5
	v_cvt_pk_fp8_f32 v9, v0, v1
	v_cvt_pk_fp8_f32 v29, v26, v27 op_sel:[0,0,1]
	v_pk_mul_f32 v[6:7], v[38:39], v[18:19] op_sel_hi:[1,0]
	v_pk_mul_f32 v[2:3], v[34:35], v[18:19] op_sel_hi:[1,0]
	v_cvt_pk_fp8_f32 v159, v156, v157 op_sel:[0,0,1]
	v_cvt_pk_fp8_f32 v147, v148, v149 op_sel:[0,0,1]
	v_cvt_pk_fp8_f32 v8, v6, v7 op_sel:[0,0,1]
	v_cvt_pk_fp8_f32 v9, v2, v3 op_sel:[0,0,1]
	s_mov_b64 s[30:31], 0x28000
	v_lshl_add_u64 v[20:21], v[16:17], 0, s[30:31]
	s_mov_b64 s[30:31], 0x2c000
	global_store_dwordx2 v[20:21], v[28:29], off offset:128
	v_lshl_add_u64 v[20:21], v[16:17], 0, s[30:31]
	s_and_b64 vcc, exec, s[38:39]
	global_store_dwordx2 v[16:17], v[158:159], off
	global_store_dwordx2 v[16:17], v[146:147], off offset:128
	global_store_dwordx2 v[20:21], v[8:9], off offset:128
	s_cbranch_vccnz .LBB0_1160
	s_andn2_b64 vcc, exec, s[28:29]
	s_cbranch_vccnz .LBB0_1159
	s_barrier
	s_branch .LBB0_1159
